# MLA loop: K fragments of the H=0 half step prefetched from LDS one half step early (behind P.V 3 of the H=1 step) into dead VGPRs
# speedup vs baseline: 1.0108x; 1.0108x over previous
.LBB0_563:
	s_or_b64 exec, exec, s[2:3]
	v_mul_f32_e32 v0, v108, v0
	v_mul_f32_e32 v1, v108, v1
	v_mul_f32_e32 v27, v108, v27
	v_mul_f32_e32 v0, v0, v114
	v_mul_f32_e32 v1, v1, v113
	v_mul_f32_e32 v27, v27, v135
	v_med3_f32 v0, v0, s69, v203
	v_med3_f32 v1, v1, s69, v203
	v_mov_b32_e32 v135, v187
	v_cvt_pk_fp8_f32 v135, v0, v1
	v_mul_f32_e32 v2, v108, v2
	v_mul_f32_e32 v3, v108, v3
	v_mul_f32_e32 v2, v2, v112
	v_mul_f32_e32 v3, v3, v111
	v_med3_f32 v0, v2, s69, v203
	v_med3_f32 v1, v3, s69, v203
	v_mul_f32_e32 v26, v108, v26
	v_cvt_pk_fp8_f32 v135, v0, v1 op_sel:[0,0,1]
	v_max_f32_e32 v0, v106, v106
	v_max_f32_e32 v1, v107, v107
	v_mul_f32_e32 v26, v26, v136
	v_med3_f32 v0, v0, s69, v203
	v_med3_f32 v1, v1, s69, v203
	v_mov_b32_e32 v136, v187
	v_cvt_pk_fp8_f32 v136, v0, v1
	v_max_f32_e32 v2, v102, v102
	v_max_f32_e32 v1, v103, v103
	v_med3_f32 v0, v2, s69, v203
	v_med3_f32 v1, v1, s69, v203
	v_mul_f32_e32 v25, v108, v25
	v_cvt_pk_fp8_f32 v136, v0, v1 op_sel:[0,0,1]
	v_max_f32_e32 v0, v100, v100
	v_max_f32_e32 v1, v101, v101
	v_mul_f32_e32 v25, v25, v137
	v_med3_f32 v0, v0, s69, v203
	v_med3_f32 v1, v1, s69, v203
	v_mov_b32_e32 v137, v187
	v_cvt_pk_fp8_f32 v137, v0, v1
	v_max_f32_e32 v2, v98, v98
	v_max_f32_e32 v1, v99, v99
	v_med3_f32 v0, v2, s69, v203
	v_med3_f32 v1, v1, s69, v203
	v_mul_f32_e32 v24, v108, v24
	v_cvt_pk_fp8_f32 v137, v0, v1 op_sel:[0,0,1]
	v_max_f32_e32 v0, v96, v96
	v_max_f32_e32 v1, v97, v97
	v_mul_f32_e32 v24, v24, v138
	v_med3_f32 v0, v0, s69, v203
	v_med3_f32 v1, v1, s69, v203
	v_mov_b32_e32 v138, v187
	v_cvt_pk_fp8_f32 v138, v0, v1
	v_max_f32_e32 v2, v94, v94
	v_max_f32_e32 v1, v95, v95
	v_med3_f32 v0, v2, s69, v203
	v_med3_f32 v1, v1, s69, v203
	v_mul_f32_e32 v31, v108, v31
	v_cvt_pk_fp8_f32 v138, v0, v1 op_sel:[0,0,1]
	v_max_f32_e32 v0, v92, v92
	v_max_f32_e32 v1, v93, v93
	v_mul_f32_e32 v31, v31, v139
	v_med3_f32 v0, v0, s69, v203
	v_med3_f32 v1, v1, s69, v203
	v_mov_b32_e32 v139, v187
	v_cvt_pk_fp8_f32 v139, v0, v1
	v_max_f32_e32 v2, v90, v90
	v_max_f32_e32 v1, v91, v91
	v_med3_f32 v0, v2, s69, v203
	v_med3_f32 v1, v1, s69, v203
	v_mul_f32_e32 v30, v108, v30
	v_cvt_pk_fp8_f32 v139, v0, v1 op_sel:[0,0,1]
	v_max_f32_e32 v0, v88, v88
	v_max_f32_e32 v1, v89, v89
	v_mul_f32_e32 v30, v30, v140
	v_med3_f32 v0, v0, s69, v203
	v_med3_f32 v1, v1, s69, v203
	v_mov_b32_e32 v140, v187
	v_cvt_pk_fp8_f32 v140, v0, v1
	v_max_f32_e32 v2, v86, v86
	v_max_f32_e32 v1, v87, v87
	v_med3_f32 v0, v2, s69, v203
	v_med3_f32 v1, v1, s69, v203
	v_mul_f32_e32 v29, v108, v29
	v_cvt_pk_fp8_f32 v140, v0, v1 op_sel:[0,0,1]
	v_max_f32_e32 v0, v84, v84
	v_max_f32_e32 v1, v85, v85
	v_mul_f32_e32 v29, v29, v141
	v_med3_f32 v0, v0, s69, v203
	v_med3_f32 v1, v1, s69, v203
	v_mov_b32_e32 v141, v187
	v_cvt_pk_fp8_f32 v141, v0, v1
	v_max_f32_e32 v2, v82, v82
	v_max_f32_e32 v1, v83, v83
	v_med3_f32 v0, v2, s69, v203
	v_med3_f32 v1, v1, s69, v203
	v_mul_f32_e32 v28, v108, v28
	v_cvt_pk_fp8_f32 v141, v0, v1 op_sel:[0,0,1]
	v_max_f32_e32 v0, v80, v80
	v_max_f32_e32 v1, v81, v81
	v_mul_f32_e32 v28, v28, v142
	v_med3_f32 v0, v0, s69, v203
	v_med3_f32 v1, v1, s69, v203
	v_mov_b32_e32 v142, v187
	v_cvt_pk_fp8_f32 v142, v0, v1
	v_mul_f32_e32 v4, v108, v4
	v_mul_f32_e32 v5, v108, v5
	v_mul_f32_e32 v60, v60, v108
	v_mul_f32_e32 v61, v61, v108
	v_mul_f32_e32 v56, v56, v108
	v_mul_f32_e32 v57, v57, v108
	v_mul_f32_e32 v52, v52, v108
	v_mul_f32_e32 v53, v108, v53
	v_mul_f32_e32 v48, v108, v48
	v_mul_f32_e32 v49, v108, v49
	v_mul_f32_e32 v44, v108, v44
	v_mul_f32_e32 v45, v108, v45
	v_mul_f32_e32 v40, v108, v40
	v_mul_f32_e32 v41, v108, v41
	v_mul_f32_e32 v36, v108, v36
	v_mul_f32_e32 v37, v108, v37
	v_mul_f32_e32 v32, v108, v32
	v_mul_f32_e32 v33, v108, v33
	v_mul_f32_e32 v20, v108, v20
	v_mul_f32_e32 v4, v4, v118
	v_mul_f32_e32 v5, v5, v117
	v_max_f32_e32 v2, v78, v78
	v_max_f32_e32 v1, v79, v79
	v_mul_f32_e32 v60, v60, v182
	v_mul_f32_e32 v61, v61, v181
	v_mul_f32_e32 v56, v56, v178
	v_mul_f32_e32 v57, v57, v177
	v_mul_f32_e32 v52, v52, v174
	v_mul_f32_e32 v53, v53, v173
	v_mul_f32_e32 v48, v48, v162
	v_mul_f32_e32 v49, v49, v161
	v_mul_f32_e32 v44, v44, v158
	v_mul_f32_e32 v45, v45, v157
	v_mul_f32_e32 v40, v40, v154
	v_mul_f32_e32 v41, v41, v153
	v_mul_f32_e32 v36, v36, v150
	v_mul_f32_e32 v37, v37, v149
	v_mul_f32_e32 v32, v32, v146
	v_mul_f32_e32 v33, v33, v145
	v_mul_f32_e32 v20, v20, v134
	v_mul_f32_e32 v19, v108, v19
	v_mul_f32_e32 v12, v108, v12
	v_mul_f32_e32 v13, v108, v13
	v_mul_f32_e32 v14, v108, v14
	v_mul_f32_e32 v15, v108, v15
	v_mul_f32_e32 v8, v108, v8
	v_mul_f32_e32 v9, v108, v9
	v_mul_f32_e32 v10, v108, v10
	v_med3_f32 v4, v4, s69, v203
	v_med3_f32 v5, v5, s69, v203
	v_mov_b32_e32 v134, v187
	v_med3_f32 v0, v2, s69, v203
	v_med3_f32 v1, v1, s69, v203
	v_mul_f32_e32 v35, v108, v35
	v_mul_f32_e32 v21, v108, v21
	v_mul_f32_e32 v19, v19, v127
	v_mul_f32_e32 v12, v12, v126
	v_mul_f32_e32 v13, v13, v125
	v_mul_f32_e32 v14, v14, v124
	v_mul_f32_e32 v15, v15, v123
	v_mul_f32_e32 v8, v8, v122
	v_mul_f32_e32 v9, v9, v121
	v_mul_f32_e32 v10, v10, v120
	v_med3_f32 v60, v60, s69, v203
	v_med3_f32 v61, v61, s69, v203
	v_mov_b32_e32 v120, v187
	v_med3_f32 v56, v56, s69, v203
	v_med3_f32 v57, v57, s69, v203
	v_mov_b32_e32 v121, v187
	v_med3_f32 v52, v52, s69, v203
	v_med3_f32 v53, v53, s69, v203
	v_mov_b32_e32 v122, v187
	v_med3_f32 v48, v48, s69, v203
	v_med3_f32 v49, v49, s69, v203
	v_mov_b32_e32 v123, v187
	v_med3_f32 v44, v44, s69, v203
	v_med3_f32 v45, v45, s69, v203
	v_mov_b32_e32 v124, v187
	v_med3_f32 v40, v40, s69, v203
	v_med3_f32 v41, v41, s69, v203
	v_mov_b32_e32 v125, v187
	v_med3_f32 v36, v36, s69, v203
	v_med3_f32 v37, v37, s69, v203
	v_mov_b32_e32 v126, v187
	v_med3_f32 v32, v32, s69, v203
	v_med3_f32 v33, v33, s69, v203
	v_mov_b32_e32 v127, v187
	v_cvt_pk_fp8_f32 v134, v4, v5
	v_cvt_pk_fp8_f32 v142, v0, v1 op_sel:[0,0,1]
	v_max_f32_e32 v0, v76, v76
	v_max_f32_e32 v1, v77, v77
	v_mul_f32_e32 v35, v35, v143
	v_mul_f32_e32 v21, v21, v133
	v_mul_f32_e32 v6, v108, v6
	v_mul_f32_e32 v7, v108, v7
	v_cvt_pk_fp8_f32 v120, v60, v61
	v_cvt_pk_fp8_f32 v121, v56, v57
	v_cvt_pk_fp8_f32 v122, v52, v53
	v_cvt_pk_fp8_f32 v123, v48, v49
	v_cvt_pk_fp8_f32 v124, v44, v45
	v_cvt_pk_fp8_f32 v125, v40, v41
	v_cvt_pk_fp8_f32 v126, v36, v37
	v_cvt_pk_fp8_f32 v127, v32, v33
	v_med3_f32 v8, v8, s69, v203
	v_med3_f32 v9, v9, s69, v203
	v_mov_b32_e32 v133, v187
	v_med3_f32 v0, v0, s69, v203
	v_med3_f32 v1, v1, s69, v203
	v_mov_b32_e32 v143, v187
	v_mul_f32_e32 v62, v62, v108
	v_mul_f32_e32 v63, v63, v108
	v_mul_f32_e32 v58, v58, v108
	v_mul_f32_e32 v59, v59, v108
	v_mul_f32_e32 v54, v108, v54
	v_mul_f32_e32 v55, v108, v55
	v_mul_f32_e32 v50, v108, v50
	v_mul_f32_e32 v51, v108, v51
	v_mul_f32_e32 v46, v108, v46
	v_mul_f32_e32 v47, v108, v47
	v_mul_f32_e32 v42, v108, v42
	v_mul_f32_e32 v43, v108, v43
	v_mul_f32_e32 v38, v108, v38
	v_mul_f32_e32 v39, v108, v39
	v_mul_f32_e32 v34, v108, v34
	v_mul_f32_e32 v16, v108, v16
	v_mul_f32_e32 v17, v108, v17
	v_mul_f32_e32 v6, v6, v116
	v_mul_f32_e32 v7, v7, v115
	v_cvt_pk_fp8_f32 v133, v8, v9
	v_cvt_pk_fp8_f32 v143, v0, v1
	v_mul_u32_u24_e32 v0, 0xd0, v186
	s_and_b32 s3, s17, 0x3fffffc0
	v_mul_f32_e32 v62, v62, v180
	v_mul_f32_e32 v63, v63, v179
	v_mul_f32_e32 v58, v58, v176
	v_mul_f32_e32 v59, v59, v175
	v_mul_f32_e32 v54, v54, v172
	v_mul_f32_e32 v55, v55, v163
	v_mul_f32_e32 v50, v50, v160
	v_mul_f32_e32 v51, v51, v159
	v_mul_f32_e32 v46, v46, v156
	v_mul_f32_e32 v47, v47, v155
	v_mul_f32_e32 v42, v42, v152
	v_mul_f32_e32 v43, v43, v151
	v_mul_f32_e32 v38, v38, v148
	v_mul_f32_e32 v39, v39, v147
	v_mul_f32_e32 v34, v34, v144
	v_mul_f32_e32 v23, v108, v23
	v_mul_f32_e32 v16, v16, v130
	v_mul_f32_e32 v17, v17, v129
	v_mul_f32_e32 v18, v108, v18
	v_mul_f32_e32 v11, v108, v11
	v_med3_f32 v6, v6, s69, v203
	v_med3_f32 v7, v7, s69, v203
	v_add3_u32 v216, 0, v0, v72
	s_lshl_b32 s3, s3, 2
	s_ashr_i32 s18, s18, 6
	v_mul_f32_e32 v23, v23, v131
	v_mul_f32_e32 v18, v18, v128
	v_mul_f32_e32 v11, v11, v119
	v_med3_f32 v62, v62, s69, v203
	v_med3_f32 v63, v63, s69, v203
	v_med3_f32 v56, v58, s69, v203
	v_med3_f32 v57, v59, s69, v203
	v_med3_f32 v54, v54, s69, v203
	v_med3_f32 v55, v55, s69, v203
	v_med3_f32 v48, v50, s69, v203
	v_med3_f32 v49, v51, s69, v203
	v_med3_f32 v46, v46, s69, v203
	v_med3_f32 v47, v47, s69, v203
	v_med3_f32 v40, v42, s69, v203
	v_med3_f32 v41, v43, s69, v203
	v_med3_f32 v38, v38, s69, v203
	v_med3_f32 v39, v39, s69, v203
	v_med3_f32 v32, v34, s69, v203
	v_med3_f32 v33, v35, s69, v203
	v_med3_f32 v28, v28, s69, v203
	v_med3_f32 v29, v29, s69, v203
	v_mov_b32_e32 v128, v187
	v_med3_f32 v24, v24, s69, v203
	v_med3_f32 v25, v25, s69, v203
	v_mov_b32_e32 v129, v187
	v_med3_f32 v20, v20, s69, v203
	v_med3_f32 v21, v21, s69, v203
	v_mov_b32_e32 v130, v187
	v_med3_f32 v16, v16, s69, v203
	v_med3_f32 v17, v17, s69, v203
	v_mov_b32_e32 v131, v187
	v_cvt_pk_fp8_f32 v134, v6, v7 op_sel:[0,0,1]
	ds_read_b128 v[0:3], v216
	ds_read_b128 v[4:7], v216 offset:16
	s_add_i32 s3, s3, 0
	s_ashr_i32 s19, s18, 31
	s_lshl_b32 s2, s74, 1
	v_cvt_pk_fp8_f32 v120, v62, v63 op_sel:[0,0,1]
	v_cvt_pk_fp8_f32 v121, v56, v57 op_sel:[0,0,1]
	v_cvt_pk_fp8_f32 v122, v54, v55 op_sel:[0,0,1]
	v_cvt_pk_fp8_f32 v123, v48, v49 op_sel:[0,0,1]
	v_cvt_pk_fp8_f32 v124, v46, v47 op_sel:[0,0,1]
	v_cvt_pk_fp8_f32 v125, v40, v41 op_sel:[0,0,1]
	v_cvt_pk_fp8_f32 v126, v38, v39 op_sel:[0,0,1]
	v_cvt_pk_fp8_f32 v127, v32, v33 op_sel:[0,0,1]
	v_cvt_pk_fp8_f32 v128, v28, v29
	v_cvt_pk_fp8_f32 v129, v24, v25
	v_cvt_pk_fp8_f32 v130, v20, v21
	v_cvt_pk_fp8_f32 v131, v16, v17
	v_med3_f32 v8, v10, s69, v203
	v_med3_f32 v9, v11, s69, v203
	s_add_i32 s79, s3, 0x18000
	s_lshl_b64 s[18:19], s[18:19], 16
	v_mul_f32_e32 v22, v108, v22
	v_cvt_pk_fp8_f32 v133, v8, v9 op_sel:[0,0,1]
	v_max_f32_e32 v8, v74, v74
	v_max_f32_e32 v9, v75, v75
	s_add_u32 s18, s44, s18
	v_mul_f32_e32 v22, v22, v132
	v_med3_f32 v8, v8, s69, v203
	v_med3_f32 v9, v9, s69, v203
	s_addc_u32 s19, s45, s19
	v_med3_f32 v30, v30, s69, v203
	v_med3_f32 v31, v31, s69, v203
	v_med3_f32 v24, v26, s69, v203
	v_med3_f32 v25, v27, s69, v203
	v_med3_f32 v22, v22, s69, v203
	v_med3_f32 v23, v23, s69, v203
	v_med3_f32 v16, v18, s69, v203
	v_med3_f32 v17, v19, s69, v203
	v_cvt_pk_fp8_f32 v143, v8, v9 op_sel:[0,0,1]
	v_lshl_add_u64 v[8:9], s[18:19], 0, v[104:105]
	v_cvt_pk_fp8_f32 v128, v30, v31 op_sel:[0,0,1]
	v_cvt_pk_fp8_f32 v129, v24, v25 op_sel:[0,0,1]
	v_cvt_pk_fp8_f32 v130, v22, v23 op_sel:[0,0,1]
	v_cvt_pk_fp8_f32 v131, v16, v17 op_sel:[0,0,1]
	s_waitcnt lgkmcnt(0)
	v_mfma_scale_f32_32x32x64_f8f6f4 v[16:31], v[0:7], v[120:127], 0, v205, v205 op_sel_hi:[0,0,0]
	ds_read_b128 v[0:3], v216 offset:64
	ds_read_b128 v[4:7], v216 offset:80
	global_load_dwordx4 v[172:175], v[8:9], off
	v_med3_f32 v12, v12, s69, v203
	v_med3_f32 v13, v13, s69, v203
	v_mov_b32_e32 v132, v187
	v_cvt_pk_fp8_f32 v132, v12, v13
	v_med3_f32 v14, v14, s69, v203
	v_med3_f32 v15, v15, s69, v203
	s_mov_b32 s17, s16
	v_cvt_pk_fp8_f32 v132, v14, v15 op_sel:[0,0,1]
	s_mov_b32 s18, s16
	s_mov_b32 s19, s16
	s_mov_b32 s20, s16
	s_mov_b32 s21, s16
	s_mov_b32 s22, s16
	s_waitcnt lgkmcnt(0)
	v_mfma_scale_f32_32x32x64_f8f6f4 v[16:31], v[0:7], v[128:135], v[16:31], v205, v205 op_sel_hi:[0,0,0]
	v_sub_u32_e32 v0, v216, v73
	ds_read_b128 v[32:35], v0 offset:128
	ds_read_b128 v[36:39], v0 offset:160
	s_mov_b32 s23, s16
	s_mov_b32 s24, s16
	s_mov_b32 s25, s16
	s_mov_b32 s26, s16
	s_mov_b32 s27, s16
	s_mov_b32 s28, s16
	s_mov_b32 s29, s16
	s_mov_b32 s30, s16
	s_mov_b32 s31, s16
	v_mov_b64_e32 v[0:1], s[16:17]
	v_and_b32_e32 v64, 63, v110
	v_mov_b64_e32 v[14:15], s[30:31]
	v_mov_b64_e32 v[2:3], s[18:19]
	s_waitcnt lgkmcnt(0)
	v_mfma_scale_f32_32x32x64_f8f6f4 v[16:31], v[32:39], v[136:143], v[16:31], v205, v205 op_sel_hi:[0,0,0]
	v_mov_b64_e32 v[4:5], s[20:21]
	v_mov_b64_e32 v[6:7], s[22:23]
	v_mov_b64_e32 v[8:9], s[24:25]
	v_mov_b64_e32 v[10:11], s[26:27]
	v_mov_b64_e32 v[12:13], s[28:29]
	v_sub_u32_e32 v217, 0, v73
	v_mov_b32_e32 v112, 0x38383838
	v_mov_b64_e32 v[62:63], v[14:15]
	s_mov_b32 s78, 2
	v_lshl_add_u32 v209, v186, 2, s79
	v_mov_b32_e32 v113, v112
	v_mov_b32_e32 v114, v112
	v_mov_b32_e32 v115, v112
	v_mov_b32_e32 v116, v112
	s_nop 5
	v_max_f32_e32 v32, v16, v17
	v_max3_f32 v32, v32, v18, v19
	v_max3_f32 v32, v32, v20, v21
	v_max3_f32 v32, v32, v22, v23
	v_max3_f32 v32, v32, v24, v25
	v_max3_f32 v32, v32, v26, v27
	v_max3_f32 v32, v32, v28, v29
	v_max3_f32 v32, v32, v30, v31
	v_mov_b32_e32 v33, v32
	s_nop 1
	v_permlane32_swap_b32_e32 v32, v33
	v_max_f32_e32 v32, v32, v33
	v_fmamk_f32 v33, v32, 0x3dd53b94, v201
	v_fmamk_f32 v32, v32, 0x3dd53b94, v202
	v_max_f32_e32 v32, 0xf149f2ca, v32
	v_cmp_ge_f32_e32 vcc, s70, v33
	v_sub_f32_e32 v33, 0xf149f2ca, v32
	s_cmp_eq_u64 vcc, exec
	v_exp_f32_e32 v33, v33
	s_cselect_b64 vcc, -1, 0
	v_cndmask_b32_e32 v192, v32, v204, vcc
	v_pk_fma_f32 v[178:179], v[16:17], s[40:41], v[192:193] op_sel_hi:[1,0,0] neg_lo:[0,0,1] neg_hi:[0,0,1]
	v_mul_u32_u24_e32 v16, 0x50, v186
	v_pk_fma_f32 v[152:153], v[30:31], s[40:41], v[192:193] op_sel_hi:[1,0,0] neg_lo:[0,0,1] neg_hi:[0,0,1]
	v_pk_fma_f32 v[154:155], v[28:29], s[40:41], v[192:193] op_sel_hi:[1,0,0] neg_lo:[0,0,1] neg_hi:[0,0,1]
	v_pk_fma_f32 v[156:157], v[26:27], s[40:41], v[192:193] op_sel_hi:[1,0,0] neg_lo:[0,0,1] neg_hi:[0,0,1]
	v_pk_fma_f32 v[158:159], v[24:25], s[40:41], v[192:193] op_sel_hi:[1,0,0] neg_lo:[0,0,1] neg_hi:[0,0,1]
	v_pk_fma_f32 v[160:161], v[22:23], s[40:41], v[192:193] op_sel_hi:[1,0,0] neg_lo:[0,0,1] neg_hi:[0,0,1]
	v_pk_fma_f32 v[162:163], v[20:21], s[40:41], v[192:193] op_sel_hi:[1,0,0] neg_lo:[0,0,1] neg_hi:[0,0,1]
	v_pk_fma_f32 v[176:177], v[18:19], s[40:41], v[192:193] op_sel_hi:[1,0,0] neg_lo:[0,0,1] neg_hi:[0,0,1]
	v_cndmask_b32_e64 v88, v33, 1.0, vcc
	v_add3_u32 v211, s67, v16, v72
	s_add_i32 s17, s2, -2
	v_cmp_gt_u32_e64 s[2:3], 32, v64
	v_mov_b64_e32 v[30:31], v[14:15]
	v_mov_b64_e32 v[46:47], v[14:15]
	v_mov_b64_e32 v[78:79], v[14:15]
	v_mov_b32_e32 v117, v112
	v_mov_b32_e32 v118, v112
	v_mov_b32_e32 v119, v112
	v_lshlrev_b32_e32 v208, 2, v109
	v_mul_lo_u32 v215, v213, s65
	v_lshl_add_u32 v214, v109, 4, s79
	s_add_i32 s20, s74, -1
	v_lshl_add_u64 v[194:195], s[4:5], 0, v[190:191]
	v_lshl_add_u64 v[196:197], s[4:5], 0, v[188:189]
	v_lshl_add_u64 v[198:199], s[44:45], 0, v[104:105]
	s_mov_b32 s21, 0
	s_movk_i32 s22, 0x80
	v_mov_b64_e32 v[28:29], v[12:13]
	v_mov_b64_e32 v[26:27], v[10:11]
	v_mov_b64_e32 v[24:25], v[8:9]
	v_mov_b64_e32 v[22:23], v[6:7]
	v_mov_b64_e32 v[20:21], v[4:5]
	v_mov_b64_e32 v[18:19], v[2:3]
	v_mov_b64_e32 v[16:17], v[0:1]
	v_mov_b64_e32 v[44:45], v[12:13]
	v_mov_b64_e32 v[42:43], v[10:11]
	v_mov_b64_e32 v[40:41], v[8:9]
	v_mov_b64_e32 v[38:39], v[6:7]
	v_mov_b64_e32 v[36:37], v[4:5]
	v_mov_b64_e32 v[34:35], v[2:3]
	v_mov_b64_e32 v[32:33], v[0:1]
	v_mov_b64_e32 v[60:61], v[12:13]
	v_mov_b64_e32 v[58:59], v[10:11]
	v_mov_b64_e32 v[56:57], v[8:9]
	v_mov_b64_e32 v[54:55], v[6:7]
	v_mov_b64_e32 v[52:53], v[4:5]
	v_mov_b64_e32 v[50:51], v[2:3]
	v_mov_b64_e32 v[48:49], v[0:1]
	v_mov_b64_e32 v[76:77], v[12:13]
	v_mov_b64_e32 v[74:75], v[10:11]
	v_mov_b64_e32 v[72:73], v[8:9]
	v_mov_b64_e32 v[70:71], v[6:7]
	v_mov_b64_e32 v[68:69], v[4:5]
	v_mov_b64_e32 v[66:67], v[2:3]
	v_mov_b64_e32 v[64:65], v[0:1]
	s_add_i32 s18, s78, -2
	s_and_b32 s23, s18, 1
	s_lshl_b32 s24, s23, 15
	v_add_u32_e32 v248, s24, v216
	ds_read_b128 v[224:227], v248 offset:6656
	ds_read_b128 v[228:231], v248 offset:6672
	ds_read_b128 v[232:235], v248 offset:6720
	ds_read_b128 v[236:239], v248 offset:6736
	v_add_u32_e32 v248, v248, v217
	ds_read_b128 v[240:243], v248 offset:6784
	ds_read_b128 v[244:247], v248 offset:6816
	s_branch .LBB0_566

.LBB0_565:
	s_waitcnt lgkmcnt(4)
	v_mfma_scale_f32_32x32x64_f8f6f4 v[96:111], v[96:103], v[120:127], 0, v205, v205 op_sel_hi:[0,0,0]
	v_cndmask_b32_e64 v176, v189, v192, s[4:5]
	v_fma_f32 v80, v80, s40, -v176
	v_fma_f32 v81, v81, s40, -v176
	v_fma_f32 v84, v84, s40, -v176
	v_fma_f32 v85, v85, s40, -v176
	v_fma_f32 v88, v88, s40, -v176
	v_fma_f32 v89, v89, s40, -v176
	v_fma_f32 v92, v92, s40, -v176
	v_fma_f32 v93, v93, s40, -v176
	v_exp_f32_e32 v80, v80
	v_exp_f32_e32 v81, v81
	v_exp_f32_e32 v84, v84
	v_exp_f32_e32 v85, v85
	v_exp_f32_e32 v88, v88
	v_exp_f32_e32 v89, v89
	s_waitcnt lgkmcnt(2)
	v_mfma_scale_f32_32x32x64_f8f6f4 v[96:111], v[156:163], v[128:135], v[96:111], v205, v205 op_sel_hi:[0,0,0]
	v_exp_f32_e32 v92, v92
	v_exp_f32_e32 v93, v93
	v_fma_f32 v82, v82, s40, -v176
	v_fma_f32 v83, v83, s40, -v176
	v_fma_f32 v86, v86, s40, -v176
	v_fma_f32 v87, v87, s40, -v176
	v_fma_f32 v90, v90, s40, -v176
	v_fma_f32 v91, v91, s40, -v176
	v_fma_f32 v94, v94, s40, -v176
	v_fma_f32 v95, v95, s40, -v176
	v_exp_f32_e32 v82, v82
	v_exp_f32_e32 v83, v83
	v_exp_f32_e32 v86, v86
	v_exp_f32_e32 v87, v87
	v_exp_f32_e32 v90, v90
	s_waitcnt lgkmcnt(0)
	v_mfma_scale_f32_32x32x64_f8f6f4 v[96:111], v[148:155], v[136:143], v[96:111], v205, v205 op_sel_hi:[0,0,0]
	v_lshl_add_u32 v240, s23, 14, v211
	ds_read_b128 v[224:227], v240
	ds_read_b128 v[228:231], v240 offset:16
	ds_read_b128 v[232:235], v240 offset:2560
	ds_read_b128 v[236:239], v240 offset:2576
	v_exp_f32_e32 v91, v91
	v_exp_f32_e32 v94, v94
	v_exp_f32_e32 v95, v95
	v_cvt_pk_fp8_f32 v148, v80, v81
	v_cvt_pk_fp8_f32 v149, v84, v85
	v_cvt_pk_fp8_f32 v150, v88, v89
	v_cvt_pk_fp8_f32 v151, v92, v93
	v_cvt_pk_fp8_f32 v148, v82, v83 op_sel:[0,0,1]
	v_cvt_pk_fp8_f32 v149, v86, v87 op_sel:[0,0,1]
	v_cvt_pk_fp8_f32 v150, v90, v91 op_sel:[0,0,1]
	v_cvt_pk_fp8_f32 v151, v94, v95 op_sel:[0,0,1]
	s_nop 0
	s_waitcnt lgkmcnt(2)
	v_mfma_scale_f32_32x32x64_f8f6f4 v[48:63], v[144:151], v[224:231], v[48:63], v205, v205 op_sel_hi:[0,0,0]
	ds_read_b128 v[80:83], v240 offset:5120
	ds_read_b128 v[84:87], v240 offset:5136
	ds_read_b128 v[152:155], v240 offset:7680
	ds_read_b128 v[156:159], v240 offset:7696
	s_waitcnt lgkmcnt(4)
	v_mfma_scale_f32_32x32x64_f8f6f4 v[32:47], v[144:151], v[232:239], v[32:47], v205, v205 op_sel_hi:[0,0,0]
	v_max_f32_e32 v88, v96, v97
	v_max3_f32 v88, v88, v98, v99
	v_max3_f32 v88, v88, v100, v101
	v_max3_f32 v88, v88, v102, v103
	v_max3_f32 v88, v88, v104, v105
	v_max3_f32 v88, v88, v106, v107
	s_waitcnt lgkmcnt(2)
	v_mfma_scale_f32_32x32x64_f8f6f4 v[16:31], v[144:151], v[80:87], v[16:31], v205, v205 op_sel_hi:[0,0,0]
	s_add_i32 s18, s78, -1
	s_and_b32 s23, s18, 1
	s_lshl_b32 s24, s23, 15
	v_add_u32_e32 v248, s24, v216
	ds_read_b128 v[224:227], v248 offset:6656
	ds_read_b128 v[228:231], v248 offset:6672
	ds_read_b128 v[232:235], v248 offset:6720
	ds_read_b128 v[236:239], v248 offset:6736
	v_add_u32_e32 v248, v248, v217
	ds_read_b128 v[240:243], v248 offset:6784
	ds_read_b128 v[244:247], v248 offset:6816
	v_max3_f32 v88, v88, v108, v109
	v_max3_f32 v88, v88, v110, v111
	v_mov_b32_e32 v89, v88
	s_nop 1
	v_permlane32_swap_b32_e32 v88, v89
	v_max_f32_e32 v80, v88, v89
	v_fma_f32 v81, v80, s40, -v176
	v_cmp_ge_f32_e32 vcc, s70, v81
	s_waitcnt lgkmcnt(6)
	v_mfma_scale_f32_32x32x64_f8f6f4 v[0:15], v[144:151], v[152:159], v[0:15], v205, v205 op_sel_hi:[0,0,0]
	s_cmp_eq_u64 vcc, exec
	s_cbranch_scc0 .Lmla_rare_a0
	v_mov_b32_e32 v192, v176
	v_mov_b32_e32 v88, 1.0

.LBB0_566:
	v_cmp_gt_f32_e32 vcc, 1.0, v88
	s_cbranch_vccz .LBB0_570
	s_and_saveexec_b64 s[4:5], s[2:3]
	ds_write_b32 v209, v88 offset:128
	s_or_b64 exec, exec, s[4:5]
	s_waitcnt lgkmcnt(0)
	ds_read_b128 v[88:91], v214 offset:224
	ds_read_b128 v[92:95], v214 offset:192
	ds_read_b128 v[144:147], v214 offset:160
	ds_read_b128 v[148:151], v214 offset:128
	s_waitcnt lgkmcnt(3)
	v_pk_mul_f32 v[62:63], v[62:63], v[90:91]
	s_waitcnt lgkmcnt(2)
	v_pk_mul_f32 v[58:59], v[58:59], v[94:95]
	s_waitcnt lgkmcnt(1)
	v_pk_mul_f32 v[54:55], v[54:55], v[146:147]
	s_waitcnt lgkmcnt(0)
	v_pk_mul_f32 v[50:51], v[50:51], v[150:151]
	v_pk_mul_f32 v[60:61], v[60:61], v[88:89]
	v_pk_mul_f32 v[56:57], v[56:57], v[92:93]
	v_pk_mul_f32 v[52:53], v[52:53], v[144:145]
	v_pk_mul_f32 v[48:49], v[48:49], v[148:149]
	v_pk_mul_f32 v[46:47], v[46:47], v[90:91]
	v_pk_mul_f32 v[42:43], v[42:43], v[94:95]
	v_pk_mul_f32 v[38:39], v[38:39], v[146:147]
	v_pk_mul_f32 v[34:35], v[34:35], v[150:151]
	v_pk_mul_f32 v[44:45], v[44:45], v[88:89]
	v_pk_mul_f32 v[40:41], v[40:41], v[92:93]
	v_pk_mul_f32 v[36:37], v[36:37], v[144:145]
	v_pk_mul_f32 v[32:33], v[32:33], v[148:149]
	v_pk_mul_f32 v[30:31], v[30:31], v[90:91]
	v_pk_mul_f32 v[26:27], v[26:27], v[94:95]
	v_pk_mul_f32 v[22:23], v[22:23], v[146:147]
	v_pk_mul_f32 v[18:19], v[18:19], v[150:151]
	v_pk_mul_f32 v[28:29], v[28:29], v[88:89]
	v_pk_mul_f32 v[24:25], v[24:25], v[92:93]
	v_pk_mul_f32 v[20:21], v[20:21], v[144:145]
	v_pk_mul_f32 v[16:17], v[16:17], v[148:149]
	v_pk_mul_f32 v[14:15], v[14:15], v[90:91]
	v_pk_mul_f32 v[10:11], v[10:11], v[94:95]
	v_pk_mul_f32 v[6:7], v[6:7], v[146:147]
	v_pk_mul_f32 v[2:3], v[2:3], v[150:151]
	v_pk_mul_f32 v[12:13], v[12:13], v[88:89]
	v_pk_mul_f32 v[8:9], v[8:9], v[92:93]
	v_pk_mul_f32 v[4:5], v[4:5], v[144:145]
	v_pk_mul_f32 v[0:1], v[0:1], v[148:149]
	v_pk_mul_f32 v[78:79], v[78:79], v[90:91]
	v_pk_mul_f32 v[74:75], v[74:75], v[94:95]
	v_pk_mul_f32 v[70:71], v[70:71], v[146:147]
	v_pk_mul_f32 v[66:67], v[66:67], v[150:151]
	v_pk_mul_f32 v[76:77], v[76:77], v[88:89]
	v_pk_mul_f32 v[72:73], v[72:73], v[92:93]
	v_pk_mul_f32 v[68:69], v[68:69], v[144:145]
	v_pk_mul_f32 v[64:65], v[64:65], v[148:149]
.LBB0_570:
	s_waitcnt lgkmcnt(4)
	v_mfma_scale_f32_32x32x64_f8f6f4 v[80:95], v[224:231], v[120:127], 0, v205, v205 op_sel_hi:[0,0,0]
	s_mov_b64 s[4:5], exec
	s_cmp_ge_u32 s18, s20
	s_waitcnt lgkmcnt(2)
	v_mfma_scale_f32_32x32x64_f8f6f4 v[80:95], v[232:239], v[128:135], v[80:95], v205, v205 op_sel_hi:[0,0,0]
	s_waitcnt lgkmcnt(0)
	v_mfma_scale_f32_32x32x64_f8f6f4 v[80:95], v[240:247], v[136:143], v[80:95], v205, v205 op_sel_hi:[0,0,0]
	s_nop 15
	s_nop 3
	v_max_f32_e32 v96, v80, v81
	v_max3_f32 v96, v96, v82, v83
	v_max3_f32 v96, v96, v84, v85
	v_max3_f32 v96, v96, v86, v87
	v_max3_f32 v96, v96, v88, v89
	v_max3_f32 v96, v96, v90, v91
	v_max3_f32 v96, v96, v92, v93
	v_max3_f32 v96, v96, v94, v95
	v_mov_b32_e32 v97, v96
	s_nop 1
	v_permlane32_swap_b32_e32 v96, v97
	v_max_f32_e32 v96, v96, v97
	v_fma_f32 v97, v96, s40, -v192
	v_cmp_ge_f32_e32 vcc, s70, v97
	s_cbranch_scc1 .LBB0_577
	s_xor_b32 s25, s23, 1
	s_lshl_b32 s18, s25, 15
	s_add_i32 s26, s18, 0
	v_add3_u32 v97, s26, v212, v190
	s_waitcnt vmcnt(1)
	ds_write_b128 v97, v[168:171]
	s_and_saveexec_b64 s[18:19], s[0:1]
	v_add3_u32 v97, s26, v215, v188
	ds_write_b128 v97, v[164:167]
	s_or_b64 exec, exec, s[18:19]
	v_lshl_add_u32 v97, s25, 14, v207
	s_cmp_ge_u32 s78, s74
	s_waitcnt vmcnt(0)
	ds_write_b128 v97, v[172:175]
	s_cbranch_scc1 .LBB0_577
	s_cmp_lt_u32 s78, s77
	s_cselect_b32 s18, 0, s77
	s_cselect_b32 s19, s76, s75
	s_lshl_b32 s18, s18, 6
	s_sub_i32 s25, s19, s18
	s_add_i32 s25, s25, s22
	v_add_u32_e32 v97, s25, v210
	v_mad_i64_i32 v[98:99], s[18:19], v97, s64, v[194:195]
	global_load_dwordx4 v[168:171], v[98:99], off
	s_and_saveexec_b64 s[18:19], s[0:1]
	s_cbranch_execz .LBB0_576
	v_add_u32_e32 v97, s25, v213
	v_mad_i64_i32 v[98:99], s[26:27], v97, s64, v[196:197]
	global_load_dwordx4 v[164:167], v[98:99], off

.LBB0_1873:
	s_or_b64 exec, exec, s[2:3]
	v_mul_f32_e32 v0, v106, v0
	v_mul_f32_e32 v1, v106, v1
	v_mul_f32_e32 v26, v106, v26
	v_mul_f32_e32 v0, v0, v113
	v_mul_f32_e32 v1, v1, v112
	v_mul_f32_e32 v26, v26, v135
	v_med3_f32 v0, v0, s67, v205
	v_med3_f32 v1, v1, s67, v205
	v_mov_b32_e32 v135, v187
	v_cvt_pk_fp8_f32 v135, v0, v1
	v_mul_f32_e32 v2, v106, v2
	v_mul_f32_e32 v3, v106, v3
	v_mul_f32_e32 v2, v2, v111
	v_mul_f32_e32 v3, v3, v110
	v_med3_f32 v0, v2, s67, v205
	v_med3_f32 v1, v3, s67, v205
	v_mul_f32_e32 v25, v106, v25
	v_cvt_pk_fp8_f32 v135, v0, v1 op_sel:[0,0,1]
	v_max_f32_e32 v0, v104, v104
	v_max_f32_e32 v1, v105, v105
	v_mul_f32_e32 v25, v25, v136
	v_med3_f32 v0, v0, s67, v205
	v_med3_f32 v1, v1, s67, v205
	v_mov_b32_e32 v136, v187
	v_cvt_pk_fp8_f32 v136, v0, v1
	v_max_f32_e32 v2, v100, v100
	v_max_f32_e32 v1, v101, v101
	v_med3_f32 v0, v2, s67, v205
	v_med3_f32 v1, v1, s67, v205
	v_mul_f32_e32 v24, v106, v24
	v_cvt_pk_fp8_f32 v136, v0, v1 op_sel:[0,0,1]
	v_max_f32_e32 v0, v98, v98
	v_max_f32_e32 v1, v99, v99
	v_mul_f32_e32 v24, v24, v137
	v_med3_f32 v0, v0, s67, v205
	v_med3_f32 v1, v1, s67, v205
	v_mov_b32_e32 v137, v187
	v_cvt_pk_fp8_f32 v137, v0, v1
	v_max_f32_e32 v2, v96, v96
	v_max_f32_e32 v1, v97, v97
	v_med3_f32 v0, v2, s67, v205
	v_med3_f32 v1, v1, s67, v205
	v_mul_f32_e32 v31, v106, v31
	v_cvt_pk_fp8_f32 v137, v0, v1 op_sel:[0,0,1]
	v_max_f32_e32 v0, v94, v94
	v_max_f32_e32 v1, v95, v95
	v_mul_f32_e32 v31, v31, v138
	v_med3_f32 v0, v0, s67, v205
	v_med3_f32 v1, v1, s67, v205
	v_mov_b32_e32 v138, v187
	v_cvt_pk_fp8_f32 v138, v0, v1
	v_max_f32_e32 v2, v92, v92
	v_max_f32_e32 v1, v93, v93
	v_med3_f32 v0, v2, s67, v205
	v_med3_f32 v1, v1, s67, v205
	v_mul_f32_e32 v30, v106, v30
	v_cvt_pk_fp8_f32 v138, v0, v1 op_sel:[0,0,1]
	v_max_f32_e32 v0, v90, v90
	v_max_f32_e32 v1, v91, v91
	v_mul_f32_e32 v30, v30, v139
	v_med3_f32 v0, v0, s67, v205
	v_med3_f32 v1, v1, s67, v205
	v_mov_b32_e32 v139, v187
	v_cvt_pk_fp8_f32 v139, v0, v1
	v_max_f32_e32 v2, v88, v88
	v_max_f32_e32 v1, v89, v89
	v_med3_f32 v0, v2, s67, v205
	v_med3_f32 v1, v1, s67, v205
	v_mul_f32_e32 v29, v106, v29
	v_cvt_pk_fp8_f32 v139, v0, v1 op_sel:[0,0,1]
	v_max_f32_e32 v0, v86, v86
	v_max_f32_e32 v1, v87, v87
	v_mul_f32_e32 v29, v29, v140
	v_med3_f32 v0, v0, s67, v205
	v_med3_f32 v1, v1, s67, v205
	v_mov_b32_e32 v140, v187
	v_cvt_pk_fp8_f32 v140, v0, v1
	v_max_f32_e32 v2, v84, v84
	v_max_f32_e32 v1, v85, v85
	v_med3_f32 v0, v2, s67, v205
	v_med3_f32 v1, v1, s67, v205
	v_mul_f32_e32 v28, v106, v28
	v_cvt_pk_fp8_f32 v140, v0, v1 op_sel:[0,0,1]
	v_max_f32_e32 v0, v82, v82
	v_max_f32_e32 v1, v83, v83
	v_mul_f32_e32 v28, v28, v141
	v_med3_f32 v0, v0, s67, v205
	v_med3_f32 v1, v1, s67, v205
	v_mov_b32_e32 v141, v187
	v_cvt_pk_fp8_f32 v141, v0, v1
	v_max_f32_e32 v2, v80, v80
	v_max_f32_e32 v1, v81, v81
	v_med3_f32 v0, v2, s67, v205
	v_med3_f32 v1, v1, s67, v205
	v_mul_f32_e32 v35, v106, v35
	v_cvt_pk_fp8_f32 v141, v0, v1 op_sel:[0,0,1]
	v_max_f32_e32 v0, v78, v78
	v_max_f32_e32 v1, v79, v79
	v_mul_f32_e32 v35, v35, v142
	v_med3_f32 v0, v0, s67, v205
	v_med3_f32 v1, v1, s67, v205
	v_mov_b32_e32 v142, v187
	v_cvt_pk_fp8_f32 v142, v0, v1
	v_mul_f32_e32 v8, v106, v8
	v_mul_f32_e32 v9, v106, v9
	v_mul_f32_e32 v4, v106, v4
	v_mul_f32_e32 v5, v106, v5
	v_mul_f32_e32 v60, v60, v106
	v_mul_f32_e32 v61, v61, v106
	v_mul_f32_e32 v56, v56, v106
	v_mul_f32_e32 v57, v57, v106
	v_mul_f32_e32 v52, v52, v106
	v_mul_f32_e32 v53, v106, v53
	v_mul_f32_e32 v48, v106, v48
	v_mul_f32_e32 v49, v106, v49
	v_mul_f32_e32 v44, v106, v44
	v_mul_f32_e32 v45, v106, v45
	v_mul_f32_e32 v40, v106, v40
	v_mul_f32_e32 v41, v106, v41
	v_mul_f32_e32 v36, v106, v36
	v_mul_f32_e32 v37, v106, v37
	v_mul_f32_e32 v32, v106, v32
	v_mul_f32_e32 v33, v106, v33
	v_mul_f32_e32 v27, v106, v27
	v_mul_f32_e32 v20, v106, v20
	v_mul_f32_e32 v8, v8, v121
	v_mul_f32_e32 v9, v9, v120
	v_mul_f32_e32 v4, v4, v117
	v_mul_f32_e32 v5, v5, v116
	v_max_f32_e32 v2, v76, v76
	v_max_f32_e32 v1, v77, v77
	v_mul_f32_e32 v60, v60, v181
	v_mul_f32_e32 v61, v61, v180
	v_mul_f32_e32 v56, v56, v177
	v_mul_f32_e32 v57, v57, v176
	v_mul_f32_e32 v52, v52, v173
	v_mul_f32_e32 v53, v53, v172
	v_mul_f32_e32 v48, v48, v161
	v_mul_f32_e32 v49, v49, v160
	v_mul_f32_e32 v44, v44, v157
	v_mul_f32_e32 v45, v45, v156
	v_mul_f32_e32 v40, v40, v153
	v_mul_f32_e32 v41, v41, v152
	v_mul_f32_e32 v36, v36, v149
	v_mul_f32_e32 v37, v37, v148
	v_mul_f32_e32 v32, v32, v145
	v_mul_f32_e32 v33, v33, v144
	v_mul_f32_e32 v27, v27, v134
	v_mul_f32_e32 v20, v20, v133
	v_mul_f32_e32 v18, v106, v18
	v_mul_f32_e32 v19, v106, v19
	v_mul_f32_e32 v12, v106, v12
	v_mul_f32_e32 v13, v106, v13
	v_mul_f32_e32 v14, v106, v14
	v_mul_f32_e32 v15, v106, v15
	v_med3_f32 v8, v8, s67, v205
	v_med3_f32 v9, v9, s67, v205
	v_mov_b32_e32 v133, v187
	v_med3_f32 v4, v4, s67, v205
	v_med3_f32 v5, v5, s67, v205
	v_mov_b32_e32 v134, v187
	v_med3_f32 v0, v2, s67, v205
	v_med3_f32 v1, v1, s67, v205
	v_mul_f32_e32 v34, v106, v34
	v_mul_f32_e32 v18, v18, v127
	v_mul_f32_e32 v19, v19, v126
	v_mul_f32_e32 v12, v12, v125
	v_mul_f32_e32 v13, v13, v124
	v_mul_f32_e32 v14, v14, v123
	v_mul_f32_e32 v15, v15, v122
	v_med3_f32 v60, v60, s67, v205
	v_med3_f32 v61, v61, s67, v205
	v_mov_b32_e32 v120, v187
	v_med3_f32 v56, v56, s67, v205
	v_med3_f32 v57, v57, s67, v205
	v_mov_b32_e32 v121, v187
	v_med3_f32 v52, v52, s67, v205
	v_med3_f32 v53, v53, s67, v205
	v_mov_b32_e32 v122, v187
	v_med3_f32 v48, v48, s67, v205
	v_med3_f32 v49, v49, s67, v205
	v_mov_b32_e32 v123, v187
	v_med3_f32 v44, v44, s67, v205
	v_med3_f32 v45, v45, s67, v205
	v_mov_b32_e32 v124, v187
	v_med3_f32 v40, v40, s67, v205
	v_med3_f32 v41, v41, s67, v205
	v_mov_b32_e32 v125, v187
	v_med3_f32 v36, v36, s67, v205
	v_med3_f32 v37, v37, s67, v205
	v_mov_b32_e32 v126, v187
	v_med3_f32 v32, v32, s67, v205
	v_med3_f32 v33, v33, s67, v205
	v_mov_b32_e32 v127, v187
	v_cvt_pk_fp8_f32 v133, v8, v9
	v_cvt_pk_fp8_f32 v134, v4, v5
	v_cvt_pk_fp8_f32 v142, v0, v1 op_sel:[0,0,1]
	v_max_f32_e32 v0, v74, v74
	v_max_f32_e32 v1, v75, v75
	s_and_b32 s2, s18, 0x3fffffc0
	v_mul_f32_e32 v34, v34, v143
	v_mul_f32_e32 v10, v106, v10
	v_mul_f32_e32 v11, v106, v11
	v_mul_f32_e32 v6, v106, v6
	v_mul_f32_e32 v7, v106, v7
	v_cvt_pk_fp8_f32 v120, v60, v61
	v_cvt_pk_fp8_f32 v121, v56, v57
	v_cvt_pk_fp8_f32 v122, v52, v53
	v_cvt_pk_fp8_f32 v123, v48, v49
	v_cvt_pk_fp8_f32 v124, v44, v45
	v_cvt_pk_fp8_f32 v125, v40, v41
	v_cvt_pk_fp8_f32 v126, v36, v37
	v_cvt_pk_fp8_f32 v127, v32, v33
	v_med3_f32 v0, v0, s67, v205
	v_med3_f32 v1, v1, s67, v205
	v_mov_b32_e32 v143, v187
	s_lshl_b32 s2, s2, 2
	v_mul_f32_e32 v62, v62, v106
	v_mul_f32_e32 v63, v63, v106
	v_mul_f32_e32 v58, v58, v106
	v_mul_f32_e32 v59, v59, v106
	v_mul_f32_e32 v54, v106, v54
	v_mul_f32_e32 v55, v106, v55
	v_mul_f32_e32 v50, v106, v50
	v_mul_f32_e32 v51, v106, v51
	v_mul_f32_e32 v46, v106, v46
	v_mul_f32_e32 v47, v106, v47
	v_mul_f32_e32 v42, v106, v42
	v_mul_f32_e32 v43, v106, v43
	v_mul_f32_e32 v38, v106, v38
	v_mul_f32_e32 v39, v106, v39
	v_mul_f32_e32 v21, v106, v21
	v_mul_f32_e32 v16, v106, v16
	v_mul_f32_e32 v17, v106, v17
	v_mul_f32_e32 v10, v10, v119
	v_mul_f32_e32 v11, v11, v118
	v_mul_f32_e32 v6, v6, v115
	v_mul_f32_e32 v7, v7, v114
	v_cvt_pk_fp8_f32 v143, v0, v1
	v_mul_u32_u24_e32 v0, 0xd0, v188
	s_add_i32 s2, s2, 0
	v_mul_f32_e32 v62, v62, v179
	v_mul_f32_e32 v63, v63, v178
	v_mul_f32_e32 v58, v58, v175
	v_mul_f32_e32 v59, v59, v174
	v_mul_f32_e32 v54, v54, v163
	v_mul_f32_e32 v55, v55, v162
	v_mul_f32_e32 v50, v50, v159
	v_mul_f32_e32 v51, v51, v158
	v_mul_f32_e32 v46, v46, v155
	v_mul_f32_e32 v47, v47, v154
	v_mul_f32_e32 v42, v42, v151
	v_mul_f32_e32 v43, v43, v150
	v_mul_f32_e32 v38, v38, v147
	v_mul_f32_e32 v39, v39, v146
	v_mul_f32_e32 v21, v21, v132
	v_mul_f32_e32 v22, v106, v22
	v_mul_f32_e32 v23, v106, v23
	v_mul_f32_e32 v16, v16, v129
	v_mul_f32_e32 v17, v17, v128
	v_med3_f32 v8, v10, s67, v205
	v_med3_f32 v9, v11, s67, v205
	v_med3_f32 v6, v6, s67, v205
	v_med3_f32 v7, v7, s67, v205
	v_max_f32_e32 v2, v72, v72
	v_add3_u32 v214, 0, v0, v186
	s_add_i32 s77, s2, 0x18000
	s_ashr_i32 s2, s19, 6
	v_mul_f32_e32 v22, v22, v131
	v_mul_f32_e32 v23, v23, v130
	v_med3_f32 v62, v62, s67, v205
	v_med3_f32 v63, v63, s67, v205
	v_med3_f32 v56, v58, s67, v205
	v_med3_f32 v57, v59, s67, v205
	v_med3_f32 v54, v54, s67, v205
	v_med3_f32 v55, v55, s67, v205
	v_med3_f32 v48, v50, s67, v205
	v_med3_f32 v49, v51, s67, v205
	v_med3_f32 v46, v46, s67, v205
	v_med3_f32 v47, v47, s67, v205
	v_med3_f32 v40, v42, s67, v205
	v_med3_f32 v41, v43, s67, v205
	v_med3_f32 v38, v38, s67, v205
	v_med3_f32 v39, v39, s67, v205
	v_med3_f32 v32, v34, s67, v205
	v_med3_f32 v33, v35, s67, v205
	v_med3_f32 v28, v28, s67, v205
	v_med3_f32 v29, v29, s67, v205
	v_mov_b32_e32 v128, v187
	v_med3_f32 v24, v24, s67, v205
	v_med3_f32 v25, v25, s67, v205
	v_mov_b32_e32 v129, v187
	v_med3_f32 v20, v20, s67, v205
	v_med3_f32 v21, v21, s67, v205
	v_mov_b32_e32 v130, v187
	v_med3_f32 v16, v16, s67, v205
	v_med3_f32 v17, v17, s67, v205
	v_mov_b32_e32 v131, v187
	v_cvt_pk_fp8_f32 v133, v8, v9 op_sel:[0,0,1]
	v_cvt_pk_fp8_f32 v134, v6, v7 op_sel:[0,0,1]
	v_med3_f32 v8, v2, s67, v205
	ds_read_b128 v[0:3], v214
	ds_read_b128 v[4:7], v214 offset:16
	s_lshl_b32 s75, s17, 8
	s_ashr_i32 s3, s2, 31
	v_cvt_pk_fp8_f32 v120, v62, v63 op_sel:[0,0,1]
	v_cvt_pk_fp8_f32 v121, v56, v57 op_sel:[0,0,1]
	v_cvt_pk_fp8_f32 v122, v54, v55 op_sel:[0,0,1]
	v_cvt_pk_fp8_f32 v123, v48, v49 op_sel:[0,0,1]
	v_cvt_pk_fp8_f32 v124, v46, v47 op_sel:[0,0,1]
	v_cvt_pk_fp8_f32 v125, v40, v41 op_sel:[0,0,1]
	v_cvt_pk_fp8_f32 v126, v38, v39 op_sel:[0,0,1]
	v_cvt_pk_fp8_f32 v127, v32, v33 op_sel:[0,0,1]
	v_cvt_pk_fp8_f32 v128, v28, v29
	v_cvt_pk_fp8_f32 v129, v24, v25
	v_cvt_pk_fp8_f32 v130, v20, v21
	v_cvt_pk_fp8_f32 v131, v16, v17
	s_addk_i32 s75, 0x2000
	s_lshl_b64 s[2:3], s[2:3], 16
	v_max_f32_e32 v9, v73, v73
	s_add_u32 s2, s40, s2
	v_med3_f32 v9, v9, s67, v205
	s_addc_u32 s3, s41, s3
	v_med3_f32 v30, v30, s67, v205
	v_med3_f32 v31, v31, s67, v205
	v_med3_f32 v24, v26, s67, v205
	v_med3_f32 v25, v27, s67, v205
	v_med3_f32 v22, v22, s67, v205
	v_med3_f32 v23, v23, s67, v205
	v_med3_f32 v16, v18, s67, v205
	v_med3_f32 v17, v19, s67, v205
	v_cvt_pk_fp8_f32 v143, v8, v9 op_sel:[0,0,1]
	v_lshl_add_u64 v[8:9], s[2:3], 0, v[102:103]
	v_cvt_pk_fp8_f32 v128, v30, v31 op_sel:[0,0,1]
	v_cvt_pk_fp8_f32 v129, v24, v25 op_sel:[0,0,1]
	v_cvt_pk_fp8_f32 v130, v22, v23 op_sel:[0,0,1]
	v_cvt_pk_fp8_f32 v131, v16, v17 op_sel:[0,0,1]
	s_waitcnt lgkmcnt(0)
	v_mfma_scale_f32_32x32x64_f8f6f4 v[16:31], v[0:7], v[120:127], 0, v207, v207 op_sel_hi:[0,0,0]
	ds_read_b128 v[0:3], v214 offset:64
	ds_read_b128 v[4:7], v214 offset:80
	global_load_dwordx4 v[172:175], v[8:9], off
	v_med3_f32 v12, v12, s67, v205
	v_med3_f32 v13, v13, s67, v205
	v_mov_b32_e32 v132, v187
	v_cvt_pk_fp8_f32 v132, v12, v13
	v_med3_f32 v14, v14, s67, v205
	v_med3_f32 v15, v15, s67, v205
	s_mov_b32 s17, s16
	v_cvt_pk_fp8_f32 v132, v14, v15 op_sel:[0,0,1]
	s_mov_b32 s18, s16
	s_mov_b32 s19, s16
	s_mov_b32 s20, s16
	s_mov_b32 s21, s16
	s_mov_b32 s22, s16
	s_waitcnt lgkmcnt(0)
	v_mfma_scale_f32_32x32x64_f8f6f4 v[16:31], v[0:7], v[128:135], v[16:31], v207, v207 op_sel_hi:[0,0,0]
	v_sub_u32_e32 v0, v214, v108
	ds_read_b128 v[32:35], v0 offset:128
	ds_read_b128 v[36:39], v0 offset:160
	s_mov_b32 s23, s16
	s_mov_b32 s24, s16
	s_mov_b32 s25, s16
	s_mov_b32 s26, s16
	s_mov_b32 s27, s16
	s_mov_b32 s28, s16
	s_mov_b32 s29, s16
	s_mov_b32 s30, s16
	s_mov_b32 s31, s16
	v_mov_b64_e32 v[0:1], s[16:17]
	v_and_b32_e32 v64, 63, v109
	v_mov_b64_e32 v[14:15], s[30:31]
	v_mov_b64_e32 v[2:3], s[18:19]
	s_waitcnt lgkmcnt(0)
	v_mfma_scale_f32_32x32x64_f8f6f4 v[16:31], v[32:39], v[136:143], v[16:31], v207, v207 op_sel_hi:[0,0,0]
	v_mov_b64_e32 v[4:5], s[20:21]
	v_mov_b64_e32 v[6:7], s[22:23]
	v_mov_b64_e32 v[8:9], s[24:25]
	v_mov_b64_e32 v[10:11], s[26:27]
	v_mov_b64_e32 v[12:13], s[28:29]
	v_mov_b32_e32 v112, 0x38383838
	v_cmp_gt_u32_e64 s[2:3], 32, v64
	v_mov_b64_e32 v[62:63], v[14:15]
	v_mov_b64_e32 v[78:79], v[14:15]
	s_mov_b32 s76, 2
	v_sub_u32_e32 v215, 0, v108
	v_lshl_add_u32 v208, v188, 2, s77
	v_mov_b32_e32 v113, v112
	v_mov_b32_e32 v114, v112
	s_nop 5
	v_max_f32_e32 v32, v16, v17
	v_max3_f32 v32, v32, v18, v19
	v_max3_f32 v32, v32, v20, v21
	v_max3_f32 v32, v32, v22, v23
	v_max3_f32 v32, v32, v24, v25
	v_max3_f32 v32, v32, v26, v27
	v_max3_f32 v32, v32, v28, v29
	v_max3_f32 v32, v32, v30, v31
	v_mov_b32_e32 v33, v32
	s_nop 1
	v_permlane32_swap_b32_e32 v32, v33
	v_max_f32_e32 v32, v32, v33
	v_fmamk_f32 v33, v32, 0x3dd53b94, v203
	v_fmamk_f32 v32, v32, 0x3dd53b94, v204
	v_max_f32_e32 v32, 0xf149f2ca, v32
	v_cmp_ge_f32_e32 vcc, s68, v33
	v_sub_f32_e32 v33, 0xf149f2ca, v32
	s_cmp_eq_u64 vcc, exec
	v_exp_f32_e32 v33, v33
	s_cselect_b64 vcc, -1, 0
	v_cndmask_b32_e32 v194, v32, v206, vcc
	v_pk_fma_f32 v[178:179], v[16:17], s[38:39], v[194:195] op_sel_hi:[1,0,0] neg_lo:[0,0,1] neg_hi:[0,0,1]
	v_mul_u32_u24_e32 v16, 0x50, v188
	v_pk_fma_f32 v[152:153], v[30:31], s[38:39], v[194:195] op_sel_hi:[1,0,0] neg_lo:[0,0,1] neg_hi:[0,0,1]
	v_pk_fma_f32 v[154:155], v[28:29], s[38:39], v[194:195] op_sel_hi:[1,0,0] neg_lo:[0,0,1] neg_hi:[0,0,1]
	v_pk_fma_f32 v[156:157], v[26:27], s[38:39], v[194:195] op_sel_hi:[1,0,0] neg_lo:[0,0,1] neg_hi:[0,0,1]
	v_pk_fma_f32 v[158:159], v[24:25], s[38:39], v[194:195] op_sel_hi:[1,0,0] neg_lo:[0,0,1] neg_hi:[0,0,1]
	v_pk_fma_f32 v[160:161], v[22:23], s[38:39], v[194:195] op_sel_hi:[1,0,0] neg_lo:[0,0,1] neg_hi:[0,0,1]
	v_pk_fma_f32 v[162:163], v[20:21], s[38:39], v[194:195] op_sel_hi:[1,0,0] neg_lo:[0,0,1] neg_hi:[0,0,1]
	v_pk_fma_f32 v[176:177], v[18:19], s[38:39], v[194:195] op_sel_hi:[1,0,0] neg_lo:[0,0,1] neg_hi:[0,0,1]
	v_cndmask_b32_e64 v88, v33, 1.0, vcc
	v_add3_u32 v209, s65, v16, v186
	v_mov_b64_e32 v[30:31], v[14:15]
	v_mov_b64_e32 v[46:47], v[14:15]
	v_mov_b32_e32 v115, v112
	v_mov_b32_e32 v116, v112
	v_mov_b32_e32 v117, v112
	v_mov_b32_e32 v118, v112
	v_mov_b32_e32 v119, v112
	v_lshlrev_b32_e32 v186, 2, v107
	v_mul_lo_u32 v216, v212, s63
	v_lshl_add_u32 v213, v107, 4, s77
	v_lshl_add_u64 v[196:197], s[4:5], 0, v[190:191]
	v_lshl_add_u64 v[198:199], s[4:5], 0, v[192:193]
	v_lshl_add_u64 v[200:201], s[40:41], 0, v[102:103]
	s_mov_b32 s17, 0
	v_mov_b64_e32 v[28:29], v[12:13]
	v_mov_b64_e32 v[26:27], v[10:11]
	v_mov_b64_e32 v[24:25], v[8:9]
	v_mov_b64_e32 v[22:23], v[6:7]
	v_mov_b64_e32 v[20:21], v[4:5]
	v_mov_b64_e32 v[18:19], v[2:3]
	v_mov_b64_e32 v[16:17], v[0:1]
	v_mov_b64_e32 v[44:45], v[12:13]
	v_mov_b64_e32 v[42:43], v[10:11]
	v_mov_b64_e32 v[40:41], v[8:9]
	v_mov_b64_e32 v[38:39], v[6:7]
	v_mov_b64_e32 v[36:37], v[4:5]
	v_mov_b64_e32 v[34:35], v[2:3]
	v_mov_b64_e32 v[32:33], v[0:1]
	v_mov_b64_e32 v[60:61], v[12:13]
	v_mov_b64_e32 v[58:59], v[10:11]
	v_mov_b64_e32 v[56:57], v[8:9]
	v_mov_b64_e32 v[54:55], v[6:7]
	v_mov_b64_e32 v[52:53], v[4:5]
	v_mov_b64_e32 v[50:51], v[2:3]
	v_mov_b64_e32 v[48:49], v[0:1]
	v_mov_b64_e32 v[76:77], v[12:13]
	v_mov_b64_e32 v[74:75], v[10:11]
	v_mov_b64_e32 v[72:73], v[8:9]
	v_mov_b64_e32 v[70:71], v[6:7]
	v_mov_b64_e32 v[68:69], v[4:5]
	v_mov_b64_e32 v[66:67], v[2:3]
	v_mov_b64_e32 v[64:65], v[0:1]
	s_add_i32 s98, s76, -2
	s_and_b32 s24, s98, 1
	s_lshl_b32 s25, s24, 15
	v_add_u32_e32 v248, s25, v214
	ds_read_b128 v[224:227], v248 offset:6656
	ds_read_b128 v[228:231], v248 offset:6672
	ds_read_b128 v[232:235], v248 offset:6720
	ds_read_b128 v[236:239], v248 offset:6736
	v_add_u32_e32 v248, v248, v215
	ds_read_b128 v[240:243], v248 offset:6784
	ds_read_b128 v[244:247], v248 offset:6816
	s_branch .LBB0_1876

.LBB0_1875:
	s_waitcnt lgkmcnt(4)
	v_mfma_scale_f32_32x32x64_f8f6f4 v[96:111], v[96:103], v[120:127], 0, v207, v207 op_sel_hi:[0,0,0]
	v_cndmask_b32_e64 v176, v191, v194, s[4:5]
	v_fma_f32 v80, v80, s38, -v176
	v_fma_f32 v81, v81, s38, -v176
	v_fma_f32 v84, v84, s38, -v176
	v_fma_f32 v85, v85, s38, -v176
	v_fma_f32 v88, v88, s38, -v176
	v_fma_f32 v89, v89, s38, -v176
	v_fma_f32 v92, v92, s38, -v176
	v_fma_f32 v93, v93, s38, -v176
	v_exp_f32_e32 v80, v80
	v_exp_f32_e32 v81, v81
	v_exp_f32_e32 v84, v84
	v_exp_f32_e32 v85, v85
	v_exp_f32_e32 v88, v88
	v_exp_f32_e32 v89, v89
	s_waitcnt lgkmcnt(2)
	v_mfma_scale_f32_32x32x64_f8f6f4 v[96:111], v[156:163], v[128:135], v[96:111], v207, v207 op_sel_hi:[0,0,0]
	v_exp_f32_e32 v92, v92
	v_exp_f32_e32 v93, v93
	v_fma_f32 v82, v82, s38, -v176
	v_fma_f32 v83, v83, s38, -v176
	v_fma_f32 v86, v86, s38, -v176
	v_fma_f32 v87, v87, s38, -v176
	v_fma_f32 v90, v90, s38, -v176
	v_fma_f32 v91, v91, s38, -v176
	v_fma_f32 v94, v94, s38, -v176
	v_fma_f32 v95, v95, s38, -v176
	v_exp_f32_e32 v82, v82
	v_exp_f32_e32 v83, v83
	v_exp_f32_e32 v86, v86
	v_exp_f32_e32 v87, v87
	v_exp_f32_e32 v90, v90
	s_waitcnt lgkmcnt(0)
	v_mfma_scale_f32_32x32x64_f8f6f4 v[96:111], v[148:155], v[136:143], v[96:111], v207, v207 op_sel_hi:[0,0,0]
	v_lshl_add_u32 v240, s24, 14, v209
	ds_read_b128 v[224:227], v240
	ds_read_b128 v[228:231], v240 offset:16
	ds_read_b128 v[232:235], v240 offset:2560
	ds_read_b128 v[236:239], v240 offset:2576
	v_exp_f32_e32 v91, v91
	v_exp_f32_e32 v94, v94
	v_exp_f32_e32 v95, v95
	v_cvt_pk_fp8_f32 v148, v80, v81
	v_cvt_pk_fp8_f32 v149, v84, v85
	v_cvt_pk_fp8_f32 v150, v88, v89
	v_cvt_pk_fp8_f32 v151, v92, v93
	v_cvt_pk_fp8_f32 v148, v82, v83 op_sel:[0,0,1]
	v_cvt_pk_fp8_f32 v149, v86, v87 op_sel:[0,0,1]
	v_cvt_pk_fp8_f32 v150, v90, v91 op_sel:[0,0,1]
	v_cvt_pk_fp8_f32 v151, v94, v95 op_sel:[0,0,1]
	s_nop 0
	s_waitcnt lgkmcnt(2)
	v_mfma_scale_f32_32x32x64_f8f6f4 v[48:63], v[144:151], v[224:231], v[48:63], v207, v207 op_sel_hi:[0,0,0]
	ds_read_b128 v[80:83], v240 offset:5120
	ds_read_b128 v[84:87], v240 offset:5136
	ds_read_b128 v[152:155], v240 offset:7680
	ds_read_b128 v[156:159], v240 offset:7696
	s_waitcnt lgkmcnt(4)
	v_mfma_scale_f32_32x32x64_f8f6f4 v[32:47], v[144:151], v[232:239], v[32:47], v207, v207 op_sel_hi:[0,0,0]
	v_max_f32_e32 v88, v96, v97
	v_max3_f32 v88, v88, v98, v99
	v_max3_f32 v88, v88, v100, v101
	v_max3_f32 v88, v88, v102, v103
	v_max3_f32 v88, v88, v104, v105
	v_max3_f32 v88, v88, v106, v107
	s_waitcnt lgkmcnt(2)
	v_mfma_scale_f32_32x32x64_f8f6f4 v[16:31], v[144:151], v[80:87], v[16:31], v207, v207 op_sel_hi:[0,0,0]
	s_add_i32 s98, s76, -1
	s_and_b32 s24, s98, 1
	s_lshl_b32 s25, s24, 15
	v_add_u32_e32 v248, s25, v214
	ds_read_b128 v[224:227], v248 offset:6656
	ds_read_b128 v[228:231], v248 offset:6672
	ds_read_b128 v[232:235], v248 offset:6720
	ds_read_b128 v[236:239], v248 offset:6736
	v_add_u32_e32 v248, v248, v215
	ds_read_b128 v[240:243], v248 offset:6784
	ds_read_b128 v[244:247], v248 offset:6816
	v_max3_f32 v88, v88, v108, v109
	v_max3_f32 v88, v88, v110, v111
	v_mov_b32_e32 v89, v88
	s_nop 1
	v_permlane32_swap_b32_e32 v88, v89
	v_max_f32_e32 v80, v88, v89
	v_fma_f32 v81, v80, s38, -v176
	v_cmp_ge_f32_e32 vcc, s68, v81
	s_waitcnt lgkmcnt(6)
	v_mfma_scale_f32_32x32x64_f8f6f4 v[0:15], v[144:151], v[152:159], v[0:15], v207, v207 op_sel_hi:[0,0,0]
	s_cmp_eq_u64 vcc, exec
	s_cbranch_scc0 .Lmla_rare_a1
	v_mov_b32_e32 v194, v176
	v_mov_b32_e32 v88, 1.0

.LBB0_1876:
	v_cmp_gt_f32_e32 vcc, 1.0, v88
	s_cbranch_vccz .LBB0_1880
	s_and_saveexec_b64 s[4:5], s[2:3]
	ds_write_b32 v208, v88 offset:128
	s_or_b64 exec, exec, s[4:5]
	s_waitcnt lgkmcnt(0)
	ds_read_b128 v[88:91], v213 offset:224
	ds_read_b128 v[92:95], v213 offset:192
	ds_read_b128 v[144:147], v213 offset:160
	ds_read_b128 v[148:151], v213 offset:128
	s_waitcnt lgkmcnt(3)
	v_pk_mul_f32 v[62:63], v[62:63], v[90:91]
	s_waitcnt lgkmcnt(2)
	v_pk_mul_f32 v[58:59], v[58:59], v[94:95]
	s_waitcnt lgkmcnt(1)
	v_pk_mul_f32 v[54:55], v[54:55], v[146:147]
	s_waitcnt lgkmcnt(0)
	v_pk_mul_f32 v[50:51], v[50:51], v[150:151]
	v_pk_mul_f32 v[60:61], v[60:61], v[88:89]
	v_pk_mul_f32 v[56:57], v[56:57], v[92:93]
	v_pk_mul_f32 v[52:53], v[52:53], v[144:145]
	v_pk_mul_f32 v[48:49], v[48:49], v[148:149]
	v_pk_mul_f32 v[46:47], v[46:47], v[90:91]
	v_pk_mul_f32 v[42:43], v[42:43], v[94:95]
	v_pk_mul_f32 v[38:39], v[38:39], v[146:147]
	v_pk_mul_f32 v[34:35], v[34:35], v[150:151]
	v_pk_mul_f32 v[44:45], v[44:45], v[88:89]
	v_pk_mul_f32 v[40:41], v[40:41], v[92:93]
	v_pk_mul_f32 v[36:37], v[36:37], v[144:145]
	v_pk_mul_f32 v[32:33], v[32:33], v[148:149]
	v_pk_mul_f32 v[30:31], v[30:31], v[90:91]
	v_pk_mul_f32 v[26:27], v[26:27], v[94:95]
	v_pk_mul_f32 v[22:23], v[22:23], v[146:147]
	v_pk_mul_f32 v[18:19], v[18:19], v[150:151]
	v_pk_mul_f32 v[28:29], v[28:29], v[88:89]
	v_pk_mul_f32 v[24:25], v[24:25], v[92:93]
	v_pk_mul_f32 v[20:21], v[20:21], v[144:145]
	v_pk_mul_f32 v[16:17], v[16:17], v[148:149]
	v_pk_mul_f32 v[14:15], v[14:15], v[90:91]
	v_pk_mul_f32 v[10:11], v[10:11], v[94:95]
	v_pk_mul_f32 v[6:7], v[6:7], v[146:147]
	v_pk_mul_f32 v[2:3], v[2:3], v[150:151]
	v_pk_mul_f32 v[12:13], v[12:13], v[88:89]
	v_pk_mul_f32 v[8:9], v[8:9], v[92:93]
	v_pk_mul_f32 v[4:5], v[4:5], v[144:145]
	v_pk_mul_f32 v[0:1], v[0:1], v[148:149]
	v_pk_mul_f32 v[78:79], v[78:79], v[90:91]
	v_pk_mul_f32 v[74:75], v[74:75], v[94:95]
	v_pk_mul_f32 v[70:71], v[70:71], v[146:147]
	v_pk_mul_f32 v[66:67], v[66:67], v[150:151]
	v_pk_mul_f32 v[76:77], v[76:77], v[88:89]
	v_pk_mul_f32 v[72:73], v[72:73], v[92:93]
	v_pk_mul_f32 v[68:69], v[68:69], v[144:145]
	v_pk_mul_f32 v[64:65], v[64:65], v[148:149]
.LBB0_1880:
	s_waitcnt lgkmcnt(4)
	v_mfma_scale_f32_32x32x64_f8f6f4 v[80:95], v[224:231], v[120:127], 0, v207, v207 op_sel_hi:[0,0,0]
	s_xor_b32 s22, s24, 1
	s_lshl_b32 s18, s22, 15
	s_add_i32 s23, s18, 0
	s_mov_b64 s[20:21], exec
	s_waitcnt lgkmcnt(2)
	v_mfma_scale_f32_32x32x64_f8f6f4 v[80:95], v[232:239], v[128:135], v[80:95], v207, v207 op_sel_hi:[0,0,0]
	s_waitcnt lgkmcnt(0)
	v_mfma_scale_f32_32x32x64_f8f6f4 v[80:95], v[240:247], v[136:143], v[80:95], v207, v207 op_sel_hi:[0,0,0]
	s_nop 15
	s_nop 3
	v_max_f32_e32 v96, v80, v81
	v_max3_f32 v96, v96, v82, v83
	v_max3_f32 v96, v96, v84, v85
	v_max3_f32 v96, v96, v86, v87
	v_max3_f32 v96, v96, v88, v89
	v_max3_f32 v96, v96, v90, v91
	v_max3_f32 v96, v96, v92, v93
	v_max3_f32 v96, v96, v94, v95
	v_mov_b32_e32 v97, v96
	s_nop 1
	v_permlane32_swap_b32_e32 v96, v97
	v_max_f32_e32 v96, v96, v97
	v_fma_f32 v97, v96, s38, -v194
	v_cmp_ge_f32_e64 s[4:5], s68, v97
	v_add3_u32 v97, s23, v210, v190
	s_waitcnt vmcnt(1)
	ds_write_b128 v97, v[168:171]
	s_and_saveexec_b64 s[18:19], s[0:1]
	v_add3_u32 v97, s23, v216, v192
	ds_write_b128 v97, v[164:167]
	s_or_b64 exec, exec, s[18:19]
	s_cmpk_gt_u32 s17, 0x83
	s_cselect_b64 s[18:19], -1, 0
	v_lshl_add_u32 v97, s22, 14, v211
	s_and_b64 vcc, exec, s[18:19]
	s_waitcnt vmcnt(0)
	ds_write_b128 v97, v[172:175]
	s_cbranch_vccnz .LBB0_1886
	s_cmpk_lt_u32 s17, 0x7c
	s_cselect_b32 s22, 0, 0xffffffc0
	s_cselect_b32 s23, s74, s75
	s_add_i32 s22, s22, s76
	s_lshl_b32 s26, s22, 6
	s_add_i32 s26, s26, s23
	v_add_u32_e32 v97, s26, v189
	v_mad_i64_i32 v[98:99], s[22:23], v97, s62, v[196:197]
	global_load_dwordx4 v[168:171], v[98:99], off
	s_and_saveexec_b64 s[22:23], s[0:1]
	s_cbranch_execz .LBB0_1885
	v_add_u32_e32 v97, s26, v212
	v_mad_i64_i32 v[98:99], s[28:29], v97, s62, v[198:199]
	global_load_dwordx4 v[164:167], v[98:99], off
